# barrier v1 with the spin-poll loops tightened (no sleep between polls)
# baseline (speedup 1.0000x reference)
; __device__ __forceinline__ unsigned xb_ld(unsigned* p)              { return __hip_atomic_load(p, __ATOMIC_RELAXED, __HIP_MEMORY_SCOPE_AGENT); }
; #define XB_SPIN(cond, bar) do { unsigned _sp = 0; while (cond) { __builtin_amdgcn_s_sleep(1); \
;     if ((++_sp & 255u) == 0u) { if (xb_ld(&(bar)[XB_TMO])) break; if (_sp > XB_SPIN_CAP) { atomicAdd(&(bar)[XB_TMO], 1u); break; } } } } while (0)
; __device__ __forceinline__ void xcd_barrier(const XcdBarrier& b) {
;     ...
;             XB_SPIN(xb_ld(&bar[XB_XGEN(b.x)]) == gen, bar);
.LBB0_37:
	s_and_b32 s22, s3, 0xff
	s_mov_b64 s[20:21], -1
	s_cmp_lg_u32 s22, 0
	s_mov_b64 s[24:25], -1
	s_nop 0
	s_cbranch_scc0 .LBB0_40
	s_and_b64 vcc, exec, s[24:25]
	s_cbranch_vccz .LBB0_36

; __device__ __forceinline__ unsigned xb_ld(unsigned* p)              { return __hip_atomic_load(p, __ATOMIC_RELAXED, __HIP_MEMORY_SCOPE_AGENT); }
; #define XB_SPIN(cond, bar) do { unsigned _sp = 0; while (cond) { __builtin_amdgcn_s_sleep(1); \
;     if ((++_sp & 255u) == 0u) { if (xb_ld(&(bar)[XB_TMO])) break; if (_sp > XB_SPIN_CAP) { atomicAdd(&(bar)[XB_TMO], 1u); break; } } } } while (0)
; __device__ __forceinline__ void xcd_barrier(const XcdBarrier& b) {
;     ...
;             else XB_SPIN(xb_ld(&bar[XB_TOPGEN]) == tg, bar);
.LBB0_54:
	s_and_b32 s20, s3, 0xff
	s_cmp_lg_u32 s20, 0
	s_mov_b64 s[22:23], -1
	s_nop 0
	s_cbranch_scc0 .LBB0_57
	s_mov_b64 s[24:25], -1
	s_and_b64 vcc, exec, s[22:23]
	s_cbranch_vccz .LBB0_53

; __device__ __forceinline__ unsigned xb_ld(unsigned* p)              { return __hip_atomic_load(p, __ATOMIC_RELAXED, __HIP_MEMORY_SCOPE_AGENT); }
; #define XB_SPIN(cond, bar) do { unsigned _sp = 0; while (cond) { __builtin_amdgcn_s_sleep(1); \
;     if ((++_sp & 255u) == 0u) { if (xb_ld(&(bar)[XB_TMO])) break; if (_sp > XB_SPIN_CAP) { atomicAdd(&(bar)[XB_TMO], 1u); break; } } } } while (0)
; __device__ __forceinline__ void xcd_barrier(const XcdBarrier& b) {
;     ...
;             XB_SPIN(xb_ld(&bar[XB_XGEN(b.x)]) == gen, bar);
.LBB0_187:
	s_and_b32 s24, s28, 0xff
	s_mov_b64 s[22:23], -1
	s_cmp_lg_u32 s24, 0
	s_mov_b64 s[26:27], -1
	s_nop 0
	s_cbranch_scc0 .LBB0_190
	s_and_b64 vcc, exec, s[26:27]
	s_cbranch_vccz .LBB0_186

; __device__ __forceinline__ unsigned xb_ld(unsigned* p)              { return __hip_atomic_load(p, __ATOMIC_RELAXED, __HIP_MEMORY_SCOPE_AGENT); }
; #define XB_SPIN(cond, bar) do { unsigned _sp = 0; while (cond) { __builtin_amdgcn_s_sleep(1); \
;     if ((++_sp & 255u) == 0u) { if (xb_ld(&(bar)[XB_TMO])) break; if (_sp > XB_SPIN_CAP) { atomicAdd(&(bar)[XB_TMO], 1u); break; } } } } while (0)
; __device__ __forceinline__ void xcd_barrier(const XcdBarrier& b) {
;     ...
;             else XB_SPIN(xb_ld(&bar[XB_TOPGEN]) == tg, bar);
.LBB0_204:
	s_and_b32 s22, s28, 0xff
	s_cmp_lg_u32 s22, 0
	s_mov_b64 s[24:25], -1
	s_nop 0
	s_cbranch_scc0 .LBB0_207
	s_mov_b64 s[26:27], -1
	s_and_b64 vcc, exec, s[24:25]
	s_cbranch_vccz .LBB0_203

; __device__ __forceinline__ unsigned xb_ld(unsigned* p)              { return __hip_atomic_load(p, __ATOMIC_RELAXED, __HIP_MEMORY_SCOPE_AGENT); }
; #define XB_SPIN(cond, bar) do { unsigned _sp = 0; while (cond) { __builtin_amdgcn_s_sleep(1); \
;     if ((++_sp & 255u) == 0u) { if (xb_ld(&(bar)[XB_TMO])) break; if (_sp > XB_SPIN_CAP) { atomicAdd(&(bar)[XB_TMO], 1u); break; } } } } while (0)
; __device__ __forceinline__ void xcd_barrier(const XcdBarrier& b) {
;     ...
;             XB_SPIN(xb_ld(&bar[XB_XGEN(b.x)]) == gen, bar);
.LBB0_630:
	s_and_b32 s22, s26, 0xff
	s_mov_b64 s[20:21], -1
	s_cmp_lg_u32 s22, 0
	s_mov_b64 s[24:25], -1
	s_nop 0
	s_cbranch_scc0 .LBB0_633
	s_and_b64 vcc, exec, s[24:25]
	s_cbranch_vccz .LBB0_629

; __device__ __forceinline__ unsigned xb_ld(unsigned* p)              { return __hip_atomic_load(p, __ATOMIC_RELAXED, __HIP_MEMORY_SCOPE_AGENT); }
; #define XB_SPIN(cond, bar) do { unsigned _sp = 0; while (cond) { __builtin_amdgcn_s_sleep(1); \
;     if ((++_sp & 255u) == 0u) { if (xb_ld(&(bar)[XB_TMO])) break; if (_sp > XB_SPIN_CAP) { atomicAdd(&(bar)[XB_TMO], 1u); break; } } } } while (0)
; __device__ __forceinline__ void xcd_barrier(const XcdBarrier& b) {
;     ...
;             else XB_SPIN(xb_ld(&bar[XB_TOPGEN]) == tg, bar);
.LBB0_647:
	s_and_b32 s20, s26, 0xff
	s_cmp_lg_u32 s20, 0
	s_mov_b64 s[22:23], -1
	s_nop 0
	s_cbranch_scc0 .LBB0_650
	s_mov_b64 s[24:25], -1
	s_and_b64 vcc, exec, s[22:23]
	s_cbranch_vccz .LBB0_646

; __device__ __forceinline__ unsigned xb_ld(unsigned* p)              { return __hip_atomic_load(p, __ATOMIC_RELAXED, __HIP_MEMORY_SCOPE_AGENT); }
; #define XB_SPIN(cond, bar) do { unsigned _sp = 0; while (cond) { __builtin_amdgcn_s_sleep(1); \
;     if ((++_sp & 255u) == 0u) { if (xb_ld(&(bar)[XB_TMO])) break; if (_sp > XB_SPIN_CAP) { atomicAdd(&(bar)[XB_TMO], 1u); break; } } } } while (0)
; __device__ __forceinline__ void xcd_barrier(const XcdBarrier& b) {
;     ...
;             XB_SPIN(xb_ld(&bar[XB_XGEN(b.x)]) == gen, bar);
.LBB0_1232:
	s_and_b32 s26, s30, 0xff
	s_mov_b64 s[24:25], -1
	s_cmp_lg_u32 s26, 0
	s_mov_b64 s[28:29], -1
	s_nop 0
	s_cbranch_scc0 .LBB0_1235
	s_and_b64 vcc, exec, s[28:29]
	s_cbranch_vccz .LBB0_1231

; __device__ __forceinline__ unsigned xb_ld(unsigned* p)              { return __hip_atomic_load(p, __ATOMIC_RELAXED, __HIP_MEMORY_SCOPE_AGENT); }
; #define XB_SPIN(cond, bar) do { unsigned _sp = 0; while (cond) { __builtin_amdgcn_s_sleep(1); \
;     if ((++_sp & 255u) == 0u) { if (xb_ld(&(bar)[XB_TMO])) break; if (_sp > XB_SPIN_CAP) { atomicAdd(&(bar)[XB_TMO], 1u); break; } } } } while (0)
; __device__ __forceinline__ void xcd_barrier(const XcdBarrier& b) {
;     ...
;             else XB_SPIN(xb_ld(&bar[XB_TOPGEN]) == tg, bar);
.LBB0_1249:
	s_and_b32 s24, s30, 0xff
	s_cmp_lg_u32 s24, 0
	s_mov_b64 s[26:27], -1
	s_nop 0
	s_cbranch_scc0 .LBB0_1252
	s_mov_b64 s[28:29], -1
	s_and_b64 vcc, exec, s[26:27]
	s_cbranch_vccz .LBB0_1248

; __device__ __forceinline__ unsigned xb_ld(unsigned* p)              { return __hip_atomic_load(p, __ATOMIC_RELAXED, __HIP_MEMORY_SCOPE_AGENT); }
; #define XB_SPIN(cond, bar) do { unsigned _sp = 0; while (cond) { __builtin_amdgcn_s_sleep(1); \
;     if ((++_sp & 255u) == 0u) { if (xb_ld(&(bar)[XB_TMO])) break; if (_sp > XB_SPIN_CAP) { atomicAdd(&(bar)[XB_TMO], 1u); break; } } } } while (0)
; __device__ __forceinline__ void xcd_barrier(const XcdBarrier& b) {
;     ...
;             XB_SPIN(xb_ld(&bar[XB_XGEN(b.x)]) == gen, bar);
.LBB0_1845:
	s_and_b32 s24, s3, 0xff
	s_mov_b64 s[22:23], -1
	s_cmp_lg_u32 s24, 0
	s_mov_b64 s[26:27], -1
	s_nop 0
	s_cbranch_scc0 .LBB0_1848
	s_and_b64 vcc, exec, s[26:27]
	s_cbranch_vccz .LBB0_1844

; __device__ __forceinline__ unsigned xb_ld(unsigned* p)              { return __hip_atomic_load(p, __ATOMIC_RELAXED, __HIP_MEMORY_SCOPE_AGENT); }
; #define XB_SPIN(cond, bar) do { unsigned _sp = 0; while (cond) { __builtin_amdgcn_s_sleep(1); \
;     if ((++_sp & 255u) == 0u) { if (xb_ld(&(bar)[XB_TMO])) break; if (_sp > XB_SPIN_CAP) { atomicAdd(&(bar)[XB_TMO], 1u); break; } } } } while (0)
; __device__ __forceinline__ void xcd_barrier(const XcdBarrier& b) {
;     ...
;             else XB_SPIN(xb_ld(&bar[XB_TOPGEN]) == tg, bar);
.LBB0_1862:
	s_and_b32 s22, s3, 0xff
	s_cmp_lg_u32 s22, 0
	s_mov_b64 s[24:25], -1
	s_nop 0
	s_cbranch_scc0 .LBB0_1865
	s_mov_b64 s[26:27], -1
	s_and_b64 vcc, exec, s[24:25]
	s_cbranch_vccz .LBB0_1861
